# speedup vs baseline: 1.0342x; 1.0021x over previous
_Z8gemm2b_kILi2EEvPKtS1_ii7EpiArgs:
	s_load_dwordx4 s[4:7], s[0:1], 0x0
	s_load_dwordx2 s[12:13], s[0:1], 0x10
	s_load_dwordx4 s[72:75], s[0:1], 0x18
	s_load_dwordx4 s[76:79], s[0:1], 0x38
	s_lshl_b32 s3, s2, 3
	s_and_b32 s3, s3, 56
	s_lshr_b32 s8, s2, 3
	s_and_b32 s9, s8, 3
	s_bfe_u32 s10, s8, 0x10005
	s_lshl_b32 s10, s10, 2
	s_or_b32 s9, s9, s10
	s_or_b32 s3, s3, s9
	s_lshl_b32 s17, s3, 7
	v_readfirstlane_b32 s19, v0
	s_waitcnt lgkmcnt(0)
	s_mul_hi_i32 s9, s13, s17
	s_mul_i32 s8, s13, s17
	s_lshr_b32 s14, s19, 6
	s_lshr_b32 s87, s2, 3
	s_bfe_u32 s88, s87, 0x30002
	s_bfe_u32 s89, s87, 0x10006
	s_lshl_b32 s89, s89, 3
	s_or_b32 s2, s88, s89
	s_ashr_i32 s11, s13, 31
	s_lshl_b64 s[8:9], s[8:9], 1
	s_mulk_i32 s2, 0xc0
	s_add_u32 s4, s4, s8
	s_addc_u32 s5, s5, s9
	s_mul_hi_i32 s9, s13, s2
	s_mul_i32 s8, s13, s2
	s_ashr_i32 s3, s2, 31
	s_lshl_b64 s[8:9], s[8:9], 1
	s_add_u32 s6, s6, s8
	s_addc_u32 s7, s7, s9
	s_lshr_b32 s8, s19, 1
	v_lshrrev_b32_e32 v1, 4, v0
	s_lshl_b32 s21, s14, 10
	s_and_b32 s16, s8, 0x7fffffc0
	v_xor_b32_e32 v3, v1, v0
	s_bitcmp1_b32 s19, 6
	v_lshrrev_b32_e32 v2, 3, v0
	v_lshlrev_b32_e32 v3, 3, v3
	s_cselect_b32 s18, 0x60, 0
	v_and_b32_e32 v186, 0x7f, v0
	v_add_u32_e32 v186, s17, v186
	v_mov_b32_e32 v187, 0
	v_lshlrev_b64 v[186:187], 5, v[186:187]
	v_lshl_add_u64 v[186:187], s[74:75], 0, v[186:187]
	global_load_dwordx4 v[188:191], v[186:187], off
	global_load_dwordx4 v[192:195], v[186:187], off offset:16
	v_lshrrev_b32_e32 v186, 2, v0
	v_and_or_b32 v186, v186, 12, s18
	v_lshlrev_b32_e32 v186, 2, v186
	s_lshl_b32 s80, s2, 2
	s_add_u32 s82, s76, s80
	s_addc_u32 s83, s77, 0
	s_add_u32 s84, s78, s80
	s_addc_u32 s85, s79, 0
	global_load_dwordx4 v[196:199], v186, s[82:83]
	global_load_dwordx4 v[200:203], v186, s[84:85]
	global_load_dwordx4 v[204:207], v186, s[82:83] offset:64
	global_load_dwordx4 v[208:211], v186, s[84:85] offset:64
	s_cmp_lg_u32 0, -1
	v_mul_lo_u32 v2, s13, v2
	v_and_b32_e32 v3, 56, v3
	s_mov_b32 s10, s13
	s_cselect_b32 s8, 0, 0
	v_add_lshl_u32 v104, v2, v3, 1
	s_add_i32 s22, s21, s8
	s_nop 4
	s_mov_b32 s8, m0
	s_mov_b32 m0, s22
	s_nop 0
	global_load_lds_dwordx4 v104, s[4:5]
	s_mov_b32 m0, s8
	s_lshl_b64 s[14:15], s[10:11], 6
	s_add_u32 s8, s4, s14
	s_addc_u32 s9, s5, s15
	s_add_i32 s23, s22, 0x1000
	s_nop 4
	s_mov_b32 s24, m0
	s_mov_b32 m0, s23
	s_nop 0
	global_load_lds_dwordx4 v104, s[8:9]
	s_mov_b32 m0, s24
	s_add_u32 s8, s8, s14
	s_addc_u32 s9, s9, s15
	s_add_i32 s24, s22, 0x2000
	s_nop 4
	s_mov_b32 s25, m0
	s_mov_b32 m0, s24
	s_nop 0
	global_load_lds_dwordx4 v104, s[8:9]
	s_mov_b32 m0, s25
	s_add_u32 s8, s8, s14
	s_addc_u32 s9, s9, s15
	s_add_i32 s25, s22, 0x3000
	s_nop 4
	s_mov_b32 s26, m0
	s_mov_b32 m0, s25
	s_nop 0
	global_load_lds_dwordx4 v104, s[8:9]
	s_mov_b32 m0, s26
	s_add_i32 s26, s22, 0x4000
	s_nop 4
	s_mov_b32 s8, m0
	s_mov_b32 m0, s26
	s_nop 0
	global_load_lds_dwordx4 v104, s[6:7]
	s_mov_b32 m0, s8
	s_add_u32 s8, s6, s14
	s_addc_u32 s9, s7, s15
	s_add_i32 s27, s22, 0x5000
	s_nop 4
	s_mov_b32 s28, m0
	s_mov_b32 m0, s27
	s_nop 0
	global_load_lds_dwordx4 v104, s[8:9]
	s_mov_b32 m0, s28
	s_add_u32 s8, s8, s14
	s_addc_u32 s9, s9, s15
	s_add_i32 s28, s22, 0x6000
	s_nop 4
	s_mov_b32 s29, m0
	s_mov_b32 m0, s28
	s_nop 0
	global_load_lds_dwordx4 v104, s[8:9]
	s_mov_b32 m0, s29
	s_add_u32 s8, s8, s14
	s_addc_u32 s9, s9, s15
	s_add_i32 s29, s22, 0x7000
	s_nop 4
	s_mov_b32 s30, m0
	s_mov_b32 m0, s29
	s_nop 0
	global_load_lds_dwordx4 v104, s[8:9]
	s_mov_b32 m0, s30
	s_add_u32 s8, s8, s14
	s_addc_u32 s9, s9, s15
	s_add_i32 s30, s22, 0x8000
	s_nop 4
	s_mov_b32 s31, m0
	s_mov_b32 m0, s30
	s_nop 0
	global_load_lds_dwordx4 v104, s[8:9]
	s_mov_b32 m0, s31
	s_add_u32 s8, s8, s14
	s_addc_u32 s9, s9, s15
	s_add_i32 s31, s22, 0x9000
	s_nop 4
	s_mov_b32 s33, m0
	s_mov_b32 m0, s31
	s_nop 0
	global_load_lds_dwordx4 v104, s[8:9]
	s_mov_b32 m0, s33
	s_ashr_i32 s13, s13, 6
	s_mov_b32 s20, 1
	s_cmp_lt_i32 s13, 1
	s_cbranch_scc1 .LBB2_7
	s_lshl_b64 s[8:9], s[10:11], 5
	s_cmp_lg_u32 0, -1
	s_cselect_b32 s33, 0, 0
	s_add_i32 s34, s33, s21
	s_add_i32 s33, s34, 0xa000
	s_add_i32 s34, s34, 0xe000
	s_lshl_b64 s[8:9], s[8:9], 1
	s_add_u32 s45, s4, s8
	s_addc_u32 s46, s5, s9
	s_add_u32 s43, s45, s14
	s_addc_u32 s44, s46, s15
	s_add_u32 s41, s43, s14
	s_addc_u32 s42, s44, s15
	s_add_u32 s35, s6, s8
	s_addc_u32 s38, s7, s9
	s_add_u32 s39, s35, s14
	s_addc_u32 s40, s38, s15
	s_add_u32 s47, s39, s14
	s_addc_u32 s48, s40, s15
	s_add_u32 s49, s47, s14
	s_addc_u32 s50, s48, s15
	s_add_u32 s51, s49, s14
	s_addc_u32 s52, s50, s15
	s_lshl_b64 s[36:37], s[10:11], 7
	s_sub_u32 s36, 0, s36
	s_subb_u32 s37, 0, s37
	s_add_u32 s61, s41, s36
	s_addc_u32 s62, s42, s37
	s_add_u32 s59, s61, s14
	s_addc_u32 s60, s62, s15
	s_add_u32 s57, s59, s14
	s_addc_u32 s58, s60, s15
	s_lshl_b64 s[10:11], s[10:11], 8
	s_sub_u32 s10, 0, s10
	s_subb_u32 s11, 0, s11
	s_add_u32 s53, s51, s10
	s_addc_u32 s54, s52, s11
	s_add_u32 s55, s53, s14
	s_addc_u32 s56, s54, s15
	s_add_u32 s63, s55, s14
	s_addc_u32 s64, s56, s15
	s_add_u32 s65, s63, s14
	s_addc_u32 s66, s64, s15
	s_add_u32 s67, s65, s14
	s_addc_u32 s68, s66, s15
	s_add_u32 s10, s35, 0x80
	s_addc_u32 s11, s38, 0
	s_add_u32 s14, s39, 0x80
	s_addc_u32 s15, s40, 0
	s_add_u32 s35, s47, 0x80
	s_addc_u32 s36, s48, 0
	s_add_u32 s37, s49, 0x80
	s_addc_u32 s38, s50, 0
	s_add_u32 s39, s51, 0x80
	s_addc_u32 s40, s52, 0
	s_add_u32 s41, s41, 0x80
	s_addc_u32 s42, s42, 0
	s_add_u32 s43, s43, 0x80
	s_addc_u32 s44, s44, 0
	s_add_u32 s45, s45, 0x80
	s_addc_u32 s46, s46, 0
	s_add_u32 s47, s53, 0x100
	s_addc_u32 s48, s54, 0
	s_add_u32 s49, s55, 0x100
	s_addc_u32 s50, s56, 0
	s_add_u32 s51, s63, 0x100
	s_addc_u32 s52, s64, 0
	s_add_u32 s53, s65, 0x100
	s_addc_u32 s54, s66, 0
	s_add_u32 s55, s67, 0x100
	s_addc_u32 s56, s68, 0
	v_and_b32_e32 v2, 15, v0
	v_bfe_u32 v0, v0, 1, 3
	s_add_u32 s57, s57, 0x100
	v_bitop3_b32 v0, v1, v0, 3 bitop3:0x6c
	s_addc_u32 s58, s58, 0
	v_lshlrev_b32_e32 v105, 4, v0
	v_or_b32_e32 v0, s18, v2
	s_add_u32 s59, s59, 0x100
	v_xor_b32_e32 v106, 64, v105
	v_lshl_add_u32 v0, v0, 7, 0
	s_addc_u32 s60, s60, 0
	v_or_b32_e32 v1, s16, v2
	v_add_u32_e32 v107, v0, v105
	v_add_u32_e32 v109, v0, v106
	s_add_u32 s61, s61, 0x100
	v_mov_b32_e32 v36, 0
	v_lshl_add_u32 v108, v1, 7, 0
	s_mov_b64 s[8:9], 0
	s_addc_u32 s62, s62, 0
	v_mov_b32_e32 v37, v36
	v_mov_b32_e32 v38, v36
	v_mov_b32_e32 v39, v36
	v_mov_b32_e32 v56, v36
	v_mov_b32_e32 v57, v36
	v_mov_b32_e32 v58, v36
	v_mov_b32_e32 v59, v36
	v_mov_b32_e32 v76, v36
	v_mov_b32_e32 v77, v36
	v_mov_b32_e32 v78, v36
	v_mov_b32_e32 v79, v36
	v_mov_b32_e32 v92, v36
	v_mov_b32_e32 v93, v36
	v_mov_b32_e32 v94, v36
	v_mov_b32_e32 v95, v36
	v_mov_b32_e32 v8, v36
	v_mov_b32_e32 v9, v36
	v_mov_b32_e32 v10, v36
	v_mov_b32_e32 v11, v36
	v_mov_b32_e32 v24, v36
	v_mov_b32_e32 v25, v36
	v_mov_b32_e32 v26, v36
	v_mov_b32_e32 v27, v36
	v_mov_b32_e32 v40, v36
	v_mov_b32_e32 v41, v36
	v_mov_b32_e32 v42, v36
	v_mov_b32_e32 v43, v36
	v_mov_b32_e32 v64, v36
	v_mov_b32_e32 v65, v36
	v_mov_b32_e32 v66, v36
	v_mov_b32_e32 v67, v36
	v_mov_b32_e32 v80, v36
	v_mov_b32_e32 v81, v36
	v_mov_b32_e32 v82, v36
	v_mov_b32_e32 v83, v36
	v_mov_b32_e32 v96, v36
	v_mov_b32_e32 v97, v36
	v_mov_b32_e32 v98, v36
	v_mov_b32_e32 v99, v36
	v_mov_b32_e32 v12, v36
	v_mov_b32_e32 v13, v36
	v_mov_b32_e32 v14, v36
	v_mov_b32_e32 v15, v36
	v_mov_b32_e32 v28, v36
	v_mov_b32_e32 v29, v36
	v_mov_b32_e32 v30, v36
	v_mov_b32_e32 v31, v36
	v_mov_b32_e32 v48, v36
	v_mov_b32_e32 v49, v36
	v_mov_b32_e32 v50, v36
	v_mov_b32_e32 v51, v36
	v_mov_b32_e32 v68, v36
	v_mov_b32_e32 v69, v36
	v_mov_b32_e32 v70, v36
	v_mov_b32_e32 v71, v36
	v_mov_b32_e32 v84, v36
	v_mov_b32_e32 v85, v36
	v_mov_b32_e32 v86, v36
	v_mov_b32_e32 v87, v36
	v_mov_b32_e32 v100, v36
	v_mov_b32_e32 v101, v36
	v_mov_b32_e32 v102, v36
	v_mov_b32_e32 v103, v36
	v_mov_b32_e32 v20, v36
	v_mov_b32_e32 v21, v36
	v_mov_b32_e32 v22, v36
	v_mov_b32_e32 v23, v36
	v_mov_b32_e32 v4, v36
	v_mov_b32_e32 v5, v36
	v_mov_b32_e32 v6, v36
	v_mov_b32_e32 v7, v36
	v_mov_b32_e32 v88, v36
	v_mov_b32_e32 v89, v36
	v_mov_b32_e32 v90, v36
	v_mov_b32_e32 v91, v36
	v_mov_b32_e32 v72, v36
	v_mov_b32_e32 v73, v36
	v_mov_b32_e32 v74, v36
	v_mov_b32_e32 v75, v36
	v_mov_b32_e32 v52, v36
	v_mov_b32_e32 v53, v36
	v_mov_b32_e32 v54, v36
	v_mov_b32_e32 v55, v36
	v_mov_b32_e32 v32, v36
	v_mov_b32_e32 v33, v36
	v_mov_b32_e32 v34, v36
	v_mov_b32_e32 v35, v36
	v_mov_b32_e32 v16, v36
	v_mov_b32_e32 v17, v36
	v_mov_b32_e32 v18, v36
	v_mov_b32_e32 v19, v36
	v_mov_b32_e32 v0, v36
	v_mov_b32_e32 v1, v36
	v_mov_b32_e32 v2, v36
	v_mov_b32_e32 v3, v36
	v_add_u32_e32 v110, 0x4000, v107
	v_add_u32_e32 v111, 0x4000, v109
	s_branch .LBB2_3

	.amdhsa_kernel _Z8gemm2b_kILi2EEvPKtS1_ii7EpiArgs
		.amdhsa_group_segment_fixed_size 0
		.amdhsa_private_segment_fixed_size 0
		.amdhsa_kernarg_size 88
		.amdhsa_user_sgpr_count 2
		.amdhsa_user_sgpr_dispatch_ptr 0
		.amdhsa_user_sgpr_queue_ptr 0
		.amdhsa_user_sgpr_kernarg_segment_ptr 1
		.amdhsa_user_sgpr_dispatch_id 0
		.amdhsa_user_sgpr_kernarg_preload_length 0
		.amdhsa_user_sgpr_kernarg_preload_offset 0
		.amdhsa_user_sgpr_private_segment_size 0
		.amdhsa_uses_dynamic_stack 0
		.amdhsa_enable_private_segment 0
		.amdhsa_system_sgpr_workgroup_id_x 1
		.amdhsa_system_sgpr_workgroup_id_y 0
		.amdhsa_system_sgpr_workgroup_id_z 0
		.amdhsa_system_sgpr_workgroup_info 0
		.amdhsa_system_vgpr_workitem_id 0
		.amdhsa_next_free_vgpr 212
		.amdhsa_next_free_sgpr 92
		.amdhsa_accum_offset 212
		.amdhsa_reserve_vcc 1
		.amdhsa_float_round_mode_32 0
		.amdhsa_float_round_mode_16_64 0
		.amdhsa_float_denorm_mode_32 3
		.amdhsa_float_denorm_mode_16_64 3
		.amdhsa_dx10_clamp 1
		.amdhsa_ieee_mode 1
		.amdhsa_fp16_overflow 0
		.amdhsa_tg_split 0
		.amdhsa_exception_fp_ieee_invalid_op 0
		.amdhsa_exception_fp_denorm_src 0
		.amdhsa_exception_fp_ieee_div_zero 0
		.amdhsa_exception_fp_ieee_overflow 0
		.amdhsa_exception_fp_ieee_underflow 0
		.amdhsa_exception_fp_ieee_inexact 0
		.amdhsa_exception_int_div_zero 0
	.end_amdhsa_kernel

amdhsa.kernels:
  - .agpr_count:     0
    .args:
      - .offset:         0
        .size:           144
        .value_kind:     by_value
    .group_segment_fixed_size: 16640
    .kernarg_segment_align: 8
    .kernarg_segment_size: 144
    .language:       OpenCL C
    .language_version:
      - 2
      - 0
    .max_flat_workgroup_size: 256
    .name:           _Z8prep_ln18PrepArgs
    .private_segment_fixed_size: 0
    .sgpr_count:     18
    .sgpr_spill_count: 0
    .symbol:         _Z8prep_ln18PrepArgs.kd
    .uniform_work_group_size: 1
    .uses_dynamic_stack: false
    .vgpr_count:     61
    .vgpr_spill_count: 0
    .wavefront_size: 64
  - .agpr_count:     0
    .args:
      - .address_space:  global
        .offset:         0
        .size:           8
        .value_kind:     global_buffer
      - .address_space:  global
        .offset:         8
        .size:           8
        .value_kind:     global_buffer
      - .address_space:  global
        .offset:         16
        .size:           8
        .value_kind:     global_buffer
      - .address_space:  global
        .offset:         24
        .size:           8
        .value_kind:     global_buffer
      - .offset:         32
        .size:           144
        .value_kind:     by_value
    .group_segment_fixed_size: 0
    .kernarg_segment_align: 8
    .kernarg_segment_size: 176
    .language:       OpenCL C
    .language_version:
      - 2
      - 0
    .max_flat_workgroup_size: 256
    .name:           _Z10attn64_fwdPKtS0_S0_Pt8PrepArgs
    .private_segment_fixed_size: 0
    .sgpr_count:     42
    .sgpr_spill_count: 0
    .symbol:         _Z10attn64_fwdPKtS0_S0_Pt8PrepArgs.kd
    .uniform_work_group_size: 1
    .uses_dynamic_stack: false
    .vgpr_count:     221
    .vgpr_spill_count: 0
    .wavefront_size: 64
  - .agpr_count:     0
    .args:
      - .address_space:  global
        .offset:         0
        .size:           8
        .value_kind:     global_buffer
      - .address_space:  global
        .offset:         8
        .size:           8
        .value_kind:     global_buffer
      - .offset:         16
        .size:           4
        .value_kind:     by_value
      - .offset:         20
        .size:           4
        .value_kind:     by_value
      - .offset:         24
        .size:           64
        .value_kind:     by_value
    .group_segment_fixed_size: 0
    .kernarg_segment_align: 8
    .kernarg_segment_size: 88
    .language:       OpenCL C
    .language_version:
      - 2
      - 0
    .max_flat_workgroup_size: 256
    .name:           _Z8gemm2b_kILi2EEvPKtS1_ii7EpiArgs
    .private_segment_fixed_size: 0
    .sgpr_count:     98
    .sgpr_spill_count: 0
    .symbol:         _Z8gemm2b_kILi2EEvPKtS1_ii7EpiArgs.kd
    .uniform_work_group_size: 1
    .uses_dynamic_stack: false
    .vgpr_count:     212
    .vgpr_spill_count: 0
    .wavefront_size: 64
  - .agpr_count:     0
    .args:
      - .address_space:  global
        .offset:         0
        .size:           8
        .value_kind:     global_buffer
      - .address_space:  global
        .offset:         8
        .size:           8
        .value_kind:     global_buffer
      - .offset:         16
        .size:           4
        .value_kind:     by_value
      - .offset:         20
        .size:           4
        .value_kind:     by_value
      - .offset:         24
        .size:           64
        .value_kind:     by_value
    .group_segment_fixed_size: 0
    .kernarg_segment_align: 8
    .kernarg_segment_size: 88
    .language:       OpenCL C
    .language_version:
      - 2
      - 0
    .max_flat_workgroup_size: 256
    .name:           _Z8gemm2b_kILi0EEvPKtS1_ii7EpiArgs
    .private_segment_fixed_size: 0
    .sgpr_count:     85
    .sgpr_spill_count: 0
    .symbol:         _Z8gemm2b_kILi0EEvPKtS1_ii7EpiArgs.kd
    .uniform_work_group_size: 1
    .uses_dynamic_stack: false
    .vgpr_count:     186
    .vgpr_spill_count: 0
    .wavefront_size: 64
  - .agpr_count:     0
    .args:
      - .address_space:  global
        .offset:         0
        .size:           8
        .value_kind:     global_buffer
      - .address_space:  global
        .offset:         8
        .size:           8
        .value_kind:     global_buffer
      - .offset:         16
        .size:           4
        .value_kind:     by_value
      - .offset:         20
        .size:           4
        .value_kind:     by_value
      - .offset:         24
        .size:           64
        .value_kind:     by_value
    .group_segment_fixed_size: 0
    .kernarg_segment_align: 8
    .kernarg_segment_size: 88
    .language:       OpenCL C
    .language_version:
      - 2
      - 0
    .max_flat_workgroup_size: 512
    .name:           _Z6gemm_kILi1ELb1ELb0ELb1ELb1ELb0EEvPKtS1_ii7EpiArgs
    .private_segment_fixed_size: 0
    .sgpr_count:     61
    .sgpr_spill_count: 0
    .symbol:         _Z6gemm_kILi1ELb1ELb0ELb1ELb1ELb0EEvPKtS1_ii7EpiArgs.kd
    .uniform_work_group_size: 1
    .uses_dynamic_stack: false
    .vgpr_count:     116
    .vgpr_spill_count: 0
    .wavefront_size: 64
  - .agpr_count:     0
    .args:
      - .address_space:  global
        .offset:         0
        .size:           8
        .value_kind:     global_buffer
      - .address_space:  global
        .offset:         8
        .size:           8
        .value_kind:     global_buffer
      - .offset:         16
        .size:           4
        .value_kind:     by_value
      - .offset:         20
        .size:           4
        .value_kind:     by_value
      - .offset:         24
        .size:           64
        .value_kind:     by_value
    .group_segment_fixed_size: 0
    .kernarg_segment_align: 8
    .kernarg_segment_size: 88
    .language:       OpenCL C
    .language_version:
      - 2
      - 0
    .max_flat_workgroup_size: 512
    .name:           _Z6gemm_kILi1ELb1ELb1ELb0ELb0ELb1EEvPKtS1_ii7EpiArgs
    .private_segment_fixed_size: 0
    .sgpr_count:     84
    .sgpr_spill_count: 0
    .symbol:         _Z6gemm_kILi1ELb1ELb1ELb0ELb0ELb1EEvPKtS1_ii7EpiArgs.kd
    .uniform_work_group_size: 1
    .uses_dynamic_stack: false
    .vgpr_count:     224
    .vgpr_spill_count: 0
    .wavefront_size: 64
